# nt on the int8 table (uq/vq) stores in ret_r1/LRU quant_finish
# speedup vs baseline: 1.0228x; 1.0019x over previous
; template <int ISV>
; __device__ __forceinline__ void quant_finish(const QRow& q, unsigned char* qtab, float* scales, int e, int lane) {
;     ...
;     amax = wave_max(amax);
;     unsigned* qp = (unsigned*)qtab + (size_t)e * 64;
;     {
;         const float inv = amax > 0.f ? 127.0f / amax : 0.f;
;         if (lane == 0) scales[e] = amax * (1.0f / 127.0f);
; #pragma unroll
;         for (int j = 0; j < 8; ++j) {
;             qp[(size_t)j * 16384 * 64 + lane] = pack_i8x4(q.v[j], inv);
;         }
.LBB0_210:
	s_or_b64 exec, exec, s[6:7]
	v_div_scale_f32 v99, s[6:7], v98, v98, s13
	v_rcp_f32_e32 v100, v99
	s_lshl_b64 s[6:7], s[64:65], 8
	s_add_i32 s4, s4, 2
	v_add_u32_e32 v188, 0x80, v188
	v_fma_f32 v101, -v99, v100, 1.0
	v_fmac_f32_e32 v100, v101, v100
	v_div_scale_f32 v101, vcc, s13, v98, s13
	v_mul_f32_e32 v102, v101, v100
	v_fma_f32 v103, -v99, v102, v101
	v_fmac_f32_e32 v102, v103, v100
	v_fma_f32 v99, -v99, v102, v101
	v_div_fmas_f32 v99, v99, v100, v102
	v_div_fixup_f32 v99, v99, v98, s13
	v_cmp_lt_f32_e32 vcc, 0, v98
	s_add_i32 s48, s48, 16
	s_nop 0
	v_cndmask_b32_e32 v100, 0, v99, vcc
	v_fmaak_f32 v90, v90, v100, 0x4b400000
	v_fmaak_f32 v91, v91, v100, 0x4b400000
	v_fmaak_f32 v92, v92, v100, 0x4b400000
	v_fmaak_f32 v93, v93, v100, 0x4b400000
	v_lshl_add_u64 v[98:99], v[182:183], 0, s[6:7]
	v_perm_b32 v90, v91, v90, s14
	v_perm_b32 v91, v93, v92, s15
	v_or_b32_e32 v92, v90, v91
	v_add_co_u32_e32 v90, vcc, s16, v98
	v_fmaak_f32 v86, v86, v100, 0x4b400000
	v_fmaak_f32 v87, v87, v100, 0x4b400000
	v_fmaak_f32 v88, v88, v100, 0x4b400000
	v_fmaak_f32 v89, v89, v100, 0x4b400000
	v_addc_co_u32_e32 v91, vcc, 0, v99, vcc
	v_perm_b32 v86, v87, v86, s14
	v_perm_b32 v87, v89, v88, s15
	v_or_b32_e32 v88, v86, v87
	v_add_co_u32_e32 v86, vcc, s10, v98
	v_fmaak_f32 v82, v82, v100, 0x4b400000
	v_fmaak_f32 v83, v83, v100, 0x4b400000
	v_fmaak_f32 v84, v84, v100, 0x4b400000
	v_fmaak_f32 v85, v85, v100, 0x4b400000
	v_addc_co_u32_e32 v87, vcc, 0, v99, vcc
	v_perm_b32 v82, v83, v82, s14
	v_perm_b32 v83, v85, v84, s15
	v_or_b32_e32 v84, v82, v83
	v_add_co_u32_e32 v82, vcc, s17, v98
	v_fmaak_f32 v78, v78, v100, 0x4b400000
	v_fmaak_f32 v79, v79, v100, 0x4b400000
	v_fmaak_f32 v80, v80, v100, 0x4b400000
	v_fmaak_f32 v81, v81, v100, 0x4b400000
	v_addc_co_u32_e32 v83, vcc, 0, v99, vcc
	v_perm_b32 v78, v79, v78, s14
	v_perm_b32 v79, v81, v80, s15
	v_or_b32_e32 v80, v78, v79
	v_add_co_u32_e32 v78, vcc, s18, v98
	v_fmaak_f32 v74, v74, v100, 0x4b400000
	v_fmaak_f32 v75, v75, v100, 0x4b400000
	v_fmaak_f32 v76, v76, v100, 0x4b400000
	v_fmaak_f32 v77, v77, v100, 0x4b400000
	v_addc_co_u32_e32 v79, vcc, 0, v99, vcc
	v_perm_b32 v74, v75, v74, s14
	v_perm_b32 v75, v77, v76, s15
	v_or_b32_e32 v76, v74, v75
	v_add_co_u32_e32 v74, vcc, s19, v98
	v_fmaak_f32 v70, v70, v100, 0x4b400000
	v_fmaak_f32 v71, v71, v100, 0x4b400000
	v_fmaak_f32 v72, v72, v100, 0x4b400000
	v_fmaak_f32 v73, v73, v100, 0x4b400000
	v_addc_co_u32_e32 v75, vcc, 0, v99, vcc
	v_perm_b32 v70, v71, v70, s14
	v_perm_b32 v71, v73, v72, s15
	v_or_b32_e32 v72, v70, v71
	v_add_co_u32_e32 v70, vcc, s20, v98
	v_fmaak_f32 v66, v66, v100, 0x4b400000
	v_fmaak_f32 v67, v67, v100, 0x4b400000
	v_fmaak_f32 v68, v68, v100, 0x4b400000
	v_fmaak_f32 v69, v69, v100, 0x4b400000
	v_addc_co_u32_e32 v71, vcc, 0, v99, vcc
	v_perm_b32 v66, v67, v66, s14
	v_perm_b32 v67, v69, v68, s15
	v_fmaak_f32 v94, v94, v100, 0x4b400000
	v_fmaak_f32 v95, v95, v100, 0x4b400000
	v_fmaak_f32 v96, v96, v100, 0x4b400000
	v_fmaak_f32 v97, v97, v100, 0x4b400000
	v_or_b32_e32 v68, v66, v67
	v_add_co_u32_e32 v66, vcc, s21, v98
	v_perm_b32 v94, v95, v94, s14
	v_perm_b32 v95, v97, v96, s15
	v_addc_co_u32_e32 v67, vcc, 0, v99, vcc
	v_or_b32_e32 v94, v94, v95
	s_and_b64 vcc, exec, s[52:53]
	global_store_dword v[98:99], v94, off nt
	global_store_dword v[90:91], v92, off nt
	global_store_dword v[86:87], v88, off nt
	global_store_dword v[82:83], v84, off nt
	global_store_dword v[78:79], v80, off nt
	global_store_dword v[74:75], v76, off nt
	global_store_dword v[70:71], v72, off nt
	global_store_dword v[66:67], v68, off nt
	s_cbranch_vccnz .LBB0_208

; template <int ISV>
; __device__ __forceinline__ void quant_finish(const QRow& q, unsigned char* qtab, float* scales, int e, int lane) {
;     float amax = 0.f;
; #pragma unroll
;     for (int j = 0; j < 8; ++j) amax = fmaxf(amax, fmaxf(fmaxf(fabsf(q.v[j].x), fabsf(q.v[j].y)), fmaxf(fabsf(q.v[j].z), fabsf(q.v[j].w))));
;     amax = wave_max(amax);
;     unsigned* qp = (unsigned*)qtab + (size_t)e * 64;
;     {
;         const float inv = amax > 0.f ? 127.0f / amax : 0.f;
;         if (lane == 0) scales[e] = amax * (1.0f / 127.0f);
; #pragma unroll
;         for (int j = 0; j < 8; ++j) {
;             qp[(size_t)j * 16384 * 64 + lane] = pack_i8x4(q.v[j], inv);
;         }
; __device__ __forceinline__ void ret_r1_phase(LAS unsigned char* lds, const bf16_t* proj, const float* cosT, const float* sinT, float* gst, int G, int b, const float* peer_v, unsigned char* vq, float* sv) {
;     ...
;             quant_finish<1>(qa, vq, sv, (unit * 8 + i) * 8 + wid, lane); quant_finish<1>(qb, vq, sv, (unit * 8 + i + 1) * 8 + wid, lane);
.LBB0_217:
	s_or_b64 exec, exec, s[6:7]
	v_div_scale_f32 v163, s[6:7], v162, v162, s13
	v_rcp_f32_e32 v164, v163
	v_div_scale_f32 v165, vcc, s13, v162, s13
	s_lshl_b64 s[6:7], s[48:49], 8
	v_fma_f32 v187, -v163, v164, 1.0
	v_fmac_f32_e32 v164, v187, v164
	v_mul_f32_e32 v187, v165, v164
	v_fma_f32 v189, -v163, v187, v165
	v_fmac_f32_e32 v187, v189, v164
	v_fma_f32 v163, -v163, v187, v165
	v_div_fmas_f32 v163, v163, v164, v187
	v_div_fixup_f32 v163, v163, v162, s13
	v_cmp_lt_f32_e32 vcc, 0, v162
	s_nop 1
	v_cndmask_b32_e32 v164, 0, v163, vcc
	v_fmaak_f32 v122, v122, v164, 0x4b400000
	v_fmaak_f32 v123, v123, v164, 0x4b400000
	v_fmaak_f32 v124, v124, v164, 0x4b400000
	v_fmaak_f32 v125, v125, v164, 0x4b400000
	v_lshl_add_u64 v[162:163], v[182:183], 0, s[6:7]
	v_perm_b32 v122, v123, v122, s14
	v_perm_b32 v123, v125, v124, s15
	v_or_b32_e32 v124, v122, v123
	v_add_co_u32_e32 v122, vcc, s16, v162
	v_fmaak_f32 v118, v118, v164, 0x4b400000
	v_fmaak_f32 v119, v119, v164, 0x4b400000
	v_fmaak_f32 v120, v120, v164, 0x4b400000
	v_fmaak_f32 v121, v121, v164, 0x4b400000
	v_addc_co_u32_e32 v123, vcc, 0, v163, vcc
	v_perm_b32 v118, v119, v118, s14
	v_perm_b32 v119, v121, v120, s15
	v_or_b32_e32 v120, v118, v119
	v_add_co_u32_e32 v118, vcc, s10, v162
	v_fmaak_f32 v114, v114, v164, 0x4b400000
	v_fmaak_f32 v115, v115, v164, 0x4b400000
	v_fmaak_f32 v116, v116, v164, 0x4b400000
	v_fmaak_f32 v117, v117, v164, 0x4b400000
	v_addc_co_u32_e32 v119, vcc, 0, v163, vcc
	v_perm_b32 v114, v115, v114, s14
	v_perm_b32 v115, v117, v116, s15
	v_or_b32_e32 v116, v114, v115
	v_add_co_u32_e32 v114, vcc, s17, v162
	v_fmaak_f32 v110, v110, v164, 0x4b400000
	v_fmaak_f32 v111, v111, v164, 0x4b400000
	v_fmaak_f32 v112, v112, v164, 0x4b400000
	v_fmaak_f32 v113, v113, v164, 0x4b400000
	v_addc_co_u32_e32 v115, vcc, 0, v163, vcc
	v_perm_b32 v110, v111, v110, s14
	v_perm_b32 v111, v113, v112, s15
	v_or_b32_e32 v112, v110, v111
	v_add_co_u32_e32 v110, vcc, s18, v162
	v_fmaak_f32 v106, v106, v164, 0x4b400000
	s_nop 0
	v_addc_co_u32_e32 v111, vcc, 0, v163, vcc
	v_fmaak_f32 v107, v107, v164, 0x4b400000
	v_fmaak_f32 v108, v108, v164, 0x4b400000
	v_fmaak_f32 v109, v109, v164, 0x4b400000
	global_store_dword v[110:111], v112, off nt
	v_perm_b32 v106, v107, v106, s14
	v_perm_b32 v107, v109, v108, s15
	s_waitcnt vmcnt(8)
	v_max_f32_e64 v109, |v97|, |v97|
	v_max_f32_e64 v110, |v96|, |v96|
	v_max_f32_e32 v109, v110, v109
	s_waitcnt vmcnt(7)
	v_max_f32_e64 v110, |v93|, |v93|
	v_max_f32_e64 v111, |v92|, |v92|
	v_max_f32_e32 v110, v111, v110
	v_max3_f32 v109, |v94|, |v95|, v109
	v_max3_f32 v110, |v90|, |v91|, v110
	v_max3_f32 v109, v109, 0, v110
	s_waitcnt vmcnt(6)
	v_max_f32_e64 v110, |v89|, |v89|
	v_max_f32_e64 v111, |v88|, |v88|
	v_max_f32_e32 v110, v111, v110
	s_waitcnt vmcnt(5)
	v_max_f32_e64 v111, |v85|, |v85|
	v_max_f32_e64 v112, |v84|, |v84|
	v_max_f32_e32 v111, v112, v111
	v_max3_f32 v110, |v86|, |v87|, v110
	v_max3_f32 v111, |v82|, |v83|, v111
	v_max3_f32 v109, v109, v110, v111
	s_waitcnt vmcnt(4)
	v_max_f32_e64 v110, |v81|, |v81|
	v_max_f32_e64 v111, |v80|, |v80|
	v_max_f32_e32 v110, v111, v110
	s_waitcnt vmcnt(3)
	v_max_f32_e64 v111, |v77|, |v77|
	v_max_f32_e64 v112, |v76|, |v76|
	v_max_f32_e32 v111, v112, v111
	v_max3_f32 v110, |v78|, |v79|, v110
	v_max3_f32 v111, |v74|, |v75|, v111
	v_max3_f32 v109, v109, v110, v111
	s_waitcnt vmcnt(2)
	v_max_f32_e64 v110, |v73|, |v73|
	v_max_f32_e64 v111, |v72|, |v72|
	v_max_f32_e32 v110, v111, v110
	s_waitcnt vmcnt(1)
	v_max_f32_e64 v111, |v69|, |v69|
	v_max_f32_e64 v112, |v68|, |v68|
	v_max_f32_e32 v111, v112, v111
	v_max3_f32 v110, |v70|, |v71|, v110
	v_max3_f32 v111, |v66|, |v67|, v111
	v_max3_f32 v109, v109, v110, v111
	ds_bpermute_b32 v110, v171, v109
	v_or_b32_e32 v108, v106, v107
	v_add_co_u32_e32 v106, vcc, s19, v162
	v_fmaak_f32 v102, v102, v164, 0x4b400000
	s_nop 0
	v_addc_co_u32_e32 v107, vcc, 0, v163, vcc
	global_store_dword v[106:107], v108, off nt
	s_waitcnt lgkmcnt(0)
	v_max_f32_e32 v106, v110, v110
	v_max_f32_e32 v106, v109, v106
	ds_bpermute_b32 v107, v173, v106
	v_fmaak_f32 v103, v103, v164, 0x4b400000
	v_fmaak_f32 v104, v104, v164, 0x4b400000
	v_fmaak_f32 v105, v105, v164, 0x4b400000
	v_perm_b32 v102, v103, v102, s14
	v_perm_b32 v103, v105, v104, s15
	v_or_b32_e32 v104, v102, v103
	s_waitcnt lgkmcnt(0)
	v_max_f32_e32 v102, v107, v107
	v_max_f32_e32 v105, v106, v102
	ds_bpermute_b32 v106, v196, v105
	v_add_co_u32_e32 v102, vcc, s20, v162
	v_fmaak_f32 v98, v98, v164, 0x4b400000
	s_nop 0
	v_addc_co_u32_e32 v103, vcc, 0, v163, vcc
	s_waitcnt lgkmcnt(0)
	v_max_f32_e32 v106, v106, v106
	v_max_f32_e32 v105, v105, v106
	ds_bpermute_b32 v106, v197, v105
	global_store_dword v[102:103], v104, off nt
	v_fmaak_f32 v99, v99, v164, 0x4b400000
	v_fmaak_f32 v100, v100, v164, 0x4b400000
	v_fmaak_f32 v101, v101, v164, 0x4b400000
	s_waitcnt lgkmcnt(0)
	v_max_f32_e32 v102, v106, v106
	v_max_f32_e32 v102, v105, v102
	ds_bpermute_b32 v103, v198, v102
	v_perm_b32 v98, v99, v98, s14
	v_perm_b32 v99, v101, v100, s15
	v_or_b32_e32 v100, v98, v99
	v_fmaak_f32 v126, v126, v164, 0x4b400000
	s_waitcnt lgkmcnt(0)
	v_max_f32_e32 v98, v103, v103
	v_max_f32_e32 v101, v102, v98
	ds_bpermute_b32 v102, v199, v101
	v_add_co_u32_e32 v98, vcc, s21, v162
	v_fmaak_f32 v127, v127, v164, 0x4b400000
	v_fmaak_f32 v128, v128, v164, 0x4b400000
	v_fmaak_f32 v129, v129, v164, 0x4b400000
	v_addc_co_u32_e32 v99, vcc, 0, v163, vcc
	v_perm_b32 v126, v127, v126, s14
	v_perm_b32 v127, v129, v128, s15
	global_store_dword v[98:99], v100, off nt
	s_waitcnt lgkmcnt(0)
	v_max_f32_e32 v98, v102, v102
	v_or_b32_e32 v126, v126, v127
	v_max_f32_e32 v98, v101, v98
	global_store_dword v[162:163], v126, off nt
	global_store_dword v[122:123], v124, off nt
	global_store_dword v[118:119], v120, off nt
	global_store_dword v[114:115], v116, off nt
	s_and_saveexec_b64 s[6:7], s[38:39]
	s_cbranch_execz .LBB0_210
	s_lshl_b64 s[22:23], s[64:65], 2
	s_add_u32 s22, s50, s22
	s_addc_u32 s23, s51, s23
	v_mul_f32_e32 v99, 0x3c010204, v98
	global_store_dword v175, v99, s[22:23]
	s_branch .LBB0_210

; template <int ISV>
; __device__ __forceinline__ void quant_finish(const QRow& q, unsigned char* qtab, float* scales, int e, int lane) {
;     ...
;     {
;         const float inv = amax > 0.f ? 127.0f / amax : 0.f;
;         if (lane == 0) scales[e] = amax * (1.0f / 127.0f);
; #pragma unroll
;         for (int j = 0; j < 8; ++j) {
;             qp[(size_t)j * 16384 * 64 + lane] = pack_i8x4(q.v[j], inv);
;         }
; template <int MODE> ...
;     ...
;         unsigned xcur[11];
; #pragma unroll
;         for (int q = 0; q < 11; ++q) xcur[q] = xnext[q];
;         const u32x4 gc0 = gnext[0], gc1 = gnext[1]; const float hin0 = hnext;
;         if (unit + G < NCH * 8) issue(unit + G);
;     ...
;         if (QUANT_IN_LRU) quant_finish<(MODE == 1 ? 1 : 0)>(qrow, P.ws + (MODE == 1 ? WS_VQ : WS_UQ), (float*)(P.ws + (MODE == 1 ? WS_SV : WS_SU)), qe, lane);
;         __syncthreads();
.LBB0_240:
	s_or_b64 exec, exec, s[6:7]
	v_div_scale_f32 v3, s[6:7], v2, v2, s14
	v_rcp_f32_e32 v4, v3
	v_div_scale_f32 v5, vcc, s14, v2, s14
	s_lshl_b64 s[6:7], s[48:49], 8
	v_fma_f32 v6, -v3, v4, 1.0
	v_fmac_f32_e32 v4, v6, v4
	v_mul_f32_e32 v6, v5, v4
	v_fma_f32 v7, -v3, v6, v5
	v_fmac_f32_e32 v6, v7, v4
	v_fma_f32 v3, -v3, v6, v5
	v_div_fmas_f32 v3, v3, v4, v6
	v_div_fixup_f32 v3, v3, v2, s14
	v_cmp_lt_f32_e32 vcc, 0, v2
	s_mov_b32 s0, 0x400000
	s_add_i32 s17, s17, s62
	v_cndmask_b32_e32 v6, 0, v3, vcc
	v_fmaak_f32 v4, v46, v6, 0x4b400000
	v_fmaak_f32 v5, v47, v6, 0x4b400000
	v_fmaak_f32 v7, v48, v6, 0x4b400000
	v_fmaak_f32 v8, v49, v6, 0x4b400000
	v_perm_b32 v4, v5, v4, s15
	v_perm_b32 v5, v8, v7, s16
	v_lshl_add_u64 v[2:3], v[88:89], 0, s[6:7]
	v_or_b32_e32 v4, v4, v5
	global_store_dword v[2:3], v4, off nt
	v_fmaak_f32 v4, v42, v6, 0x4b400000
	v_fmaak_f32 v5, v43, v6, 0x4b400000
	v_fmaak_f32 v7, v44, v6, 0x4b400000
	v_fmaak_f32 v8, v45, v6, 0x4b400000
	v_perm_b32 v4, v5, v4, s15
	v_perm_b32 v5, v8, v7, s16
	v_or_b32_e32 v7, v4, v5
	v_add_co_u32_e32 v4, vcc, s0, v2
	v_fmaak_f32 v8, v41, v6, 0x4b400000
	s_nop 0
	v_addc_co_u32_e32 v5, vcc, 0, v3, vcc
	global_store_dword v[4:5], v7, off nt
	v_fmaak_f32 v4, v38, v6, 0x4b400000
	v_fmaak_f32 v5, v39, v6, 0x4b400000
	v_fmaak_f32 v7, v40, v6, 0x4b400000
	v_perm_b32 v4, v5, v4, s15
	v_perm_b32 v5, v8, v7, s16
	s_mov_b32 s0, 0x800000
	v_or_b32_e32 v7, v4, v5
	v_add_co_u32_e32 v4, vcc, s0, v2
	v_fmaak_f32 v8, v37, v6, 0x4b400000
	s_nop 0
	v_addc_co_u32_e32 v5, vcc, 0, v3, vcc
	global_store_dword v[4:5], v7, off nt
	v_fmaak_f32 v4, v34, v6, 0x4b400000
	v_fmaak_f32 v5, v35, v6, 0x4b400000
	v_fmaak_f32 v7, v36, v6, 0x4b400000
	v_perm_b32 v4, v5, v4, s15
	v_perm_b32 v5, v8, v7, s16
	s_mov_b32 s0, 0xc00000
	v_or_b32_e32 v7, v4, v5
	v_add_co_u32_e32 v4, vcc, s0, v2
	v_fmaak_f32 v8, v33, v6, 0x4b400000
	s_nop 0
	v_addc_co_u32_e32 v5, vcc, 0, v3, vcc
	global_store_dword v[4:5], v7, off nt
	v_fmaak_f32 v4, v30, v6, 0x4b400000
	v_fmaak_f32 v5, v31, v6, 0x4b400000
	v_fmaak_f32 v7, v32, v6, 0x4b400000
	v_perm_b32 v4, v5, v4, s15
	v_perm_b32 v5, v8, v7, s16
	s_mov_b32 s0, 0x1000000
	v_or_b32_e32 v7, v4, v5
	v_add_co_u32_e32 v4, vcc, s0, v2
	v_fmaak_f32 v8, v29, v6, 0x4b400000
	s_nop 0
	v_addc_co_u32_e32 v5, vcc, 0, v3, vcc
	global_store_dword v[4:5], v7, off nt
	v_fmaak_f32 v4, v26, v6, 0x4b400000
	v_fmaak_f32 v5, v27, v6, 0x4b400000
	v_fmaak_f32 v7, v28, v6, 0x4b400000
	v_perm_b32 v4, v5, v4, s15
	v_perm_b32 v5, v8, v7, s16
	s_mov_b32 s0, 0x1400000
	v_or_b32_e32 v7, v4, v5
	v_add_co_u32_e32 v4, vcc, s0, v2
	v_fmaak_f32 v8, v25, v6, 0x4b400000
	s_nop 0
	v_addc_co_u32_e32 v5, vcc, 0, v3, vcc
	global_store_dword v[4:5], v7, off nt
	v_fmaak_f32 v4, v22, v6, 0x4b400000
	v_fmaak_f32 v5, v23, v6, 0x4b400000
	v_fmaak_f32 v7, v24, v6, 0x4b400000
	v_perm_b32 v4, v5, v4, s15
	v_perm_b32 v5, v8, v7, s16
	s_mov_b32 s0, 0x1800000
	v_or_b32_e32 v7, v4, v5
	v_add_co_u32_e32 v4, vcc, s0, v2
	s_add_i32 s67, s67, s89
	s_nop 0
	v_addc_co_u32_e32 v5, vcc, 0, v3, vcc
	global_store_dword v[4:5], v7, off nt
	v_fmaak_f32 v4, v18, v6, 0x4b400000
	v_fmaak_f32 v5, v19, v6, 0x4b400000
	v_fmaak_f32 v7, v20, v6, 0x4b400000
	v_fmaak_f32 v6, v21, v6, 0x4b400000
	v_perm_b32 v4, v5, v4, s15
	v_perm_b32 v5, v6, v7, s16
	v_add_co_u32_e32 v2, vcc, 0x1c00000, v2
	v_or_b32_e32 v4, v4, v5
	s_nop 0
	v_addc_co_u32_e32 v3, vcc, 0, v3, vcc
	global_store_dword v[2:3], v4, off nt
	v_mov_b64_e32 v[2:3], v[14:15]
	v_mov_b64_e32 v[6:7], v[10:11]
	s_andn2_b64 vcc, exec, s[4:5]
	v_mov_b32_e32 v60, v188
	v_mov_b32_e32 v59, v187
	v_mov_b32_e32 v58, v186
	v_mov_b32_e32 v54, v184
	v_mov_b32_e32 v57, v185
	v_mov_b32_e32 v56, v183
	v_mov_b32_e32 v55, v182
	v_mov_b32_e32 v53, v181
	v_mov_b32_e32 v52, v180
	v_mov_b32_e32 v50, v178
	v_mov_b32_e32 v51, v179
	s_mov_b32 s21, s20
	v_mov_b64_e32 v[4:5], v[16:17]
	v_mov_b64_e32 v[8:9], v[12:13]
	s_barrier
	s_cbranch_vccz .LBB0_277
